# v056 + select ballots read SGPR masks directly in the remaining single-step, emit and bin-search code (88 sites)
# baseline (speedup 1.0000x reference)
.LBB0_1137:
	v_and_b32_e32 v7, 0xffff, v62
	v_add_u32_e32 v6, 0x100, v2
	v_lshrrev_b32_e32 v5, 16, v62
	v_cmp_gt_u32_e64 s[44:45], s11, v6
	v_cmp_le_u32_e32 vcc, s93, v7
	v_cmp_le_u32_e64 s[46:47], s93, v5
	s_and_b64 s[18:19], s[44:45], vcc
	v_cndmask_b32_e64 v0, 0, 1, s[18:19]
	s_and_b64 s[8:9], s[44:45], s[46:47]
	s_mov_b64 vcc, s[18:19]
	s_mov_b64 s[44:45], s[8:9]
	v_mbcnt_lo_u32_b32 v3, vcc_lo, 0
	v_mbcnt_hi_u32_b32 v3, vcc_hi, v3
	v_mbcnt_lo_u32_b32 v3, s44, v3
	s_min_u32 s46, s49, 0x2c0
	v_mbcnt_hi_u32_b32 v3, s45, v3
	s_lshl_b32 s47, s46, 3
	s_sub_i32 s59, 0x2c0, s46
	s_add_i32 s58, s88, s47
	v_cmp_gt_u32_e64 s[46:47], s59, v3
	s_and_b64 s[18:19], s[18:19], s[46:47]
	s_and_saveexec_b64 s[46:47], s[18:19]
	v_lshl_add_u32 v4, v3, 3, s58
	ds_write_b64 v4, v[6:7]
	s_or_b64 exec, exec, s[46:47]
	v_add_u32_e32 v0, v3, v0
	v_cmp_gt_u32_e64 s[46:47], s59, v0
	s_and_b64 s[18:19], s[8:9], s[46:47]
	s_and_saveexec_b64 s[8:9], s[18:19]
	v_lshl_add_u32 v0, v0, 3, s58
	v_add_u32_e32 v4, 0x101, v2
	ds_write_b64 v0, v[4:5]
	s_or_b64 exec, exec, s[8:9]
	s_bcnt1_i32_b64 s8, vcc
	s_bcnt1_i32_b64 s9, s[44:45]
	s_add_i32 s8, s49, s8
	s_add_i32 s49, s8, s9

.LBB0_1147:
	v_and_b32_e32 v7, 0xffff, v58
	v_add_u32_e32 v6, 0x200, v2
	v_lshrrev_b32_e32 v5, 16, v58
	v_cmp_gt_u32_e64 s[44:45], s11, v6
	v_cmp_le_u32_e32 vcc, s93, v7
	v_cmp_le_u32_e64 s[46:47], s93, v5
	s_and_b64 s[18:19], s[44:45], vcc
	v_cndmask_b32_e64 v0, 0, 1, s[18:19]
	s_and_b64 s[8:9], s[44:45], s[46:47]
	s_mov_b64 vcc, s[18:19]
	s_mov_b64 s[44:45], s[8:9]
	v_mbcnt_lo_u32_b32 v3, vcc_lo, 0
	v_mbcnt_hi_u32_b32 v3, vcc_hi, v3
	v_mbcnt_lo_u32_b32 v3, s44, v3
	s_min_u32 s46, s49, 0x2c0
	v_mbcnt_hi_u32_b32 v3, s45, v3
	s_lshl_b32 s47, s46, 3
	s_sub_i32 s59, 0x2c0, s46
	s_add_i32 s58, s88, s47
	v_cmp_gt_u32_e64 s[46:47], s59, v3
	s_and_b64 s[18:19], s[18:19], s[46:47]
	s_and_saveexec_b64 s[46:47], s[18:19]
	v_lshl_add_u32 v4, v3, 3, s58
	ds_write_b64 v4, v[6:7]
	s_or_b64 exec, exec, s[46:47]
	v_add_u32_e32 v0, v3, v0
	v_cmp_gt_u32_e64 s[46:47], s59, v0
	s_and_b64 s[18:19], s[8:9], s[46:47]
	s_and_saveexec_b64 s[8:9], s[18:19]
	v_lshl_add_u32 v0, v0, 3, s58
	v_add_u32_e32 v4, 0x201, v2
	ds_write_b64 v0, v[4:5]
	s_or_b64 exec, exec, s[8:9]
	s_bcnt1_i32_b64 s8, vcc
	s_bcnt1_i32_b64 s9, s[44:45]
	s_add_i32 s8, s49, s8
	s_add_i32 s49, s8, s9

.LBB0_1157:
	v_and_b32_e32 v7, 0xffff, v56
	v_add_u32_e32 v6, 0x300, v2
	v_lshrrev_b32_e32 v5, 16, v56
	v_cmp_gt_u32_e64 s[44:45], s11, v6
	v_cmp_le_u32_e32 vcc, s93, v7
	v_cmp_le_u32_e64 s[46:47], s93, v5
	s_and_b64 s[18:19], s[44:45], vcc
	v_cndmask_b32_e64 v0, 0, 1, s[18:19]
	s_and_b64 s[8:9], s[44:45], s[46:47]
	s_mov_b64 vcc, s[18:19]
	s_mov_b64 s[44:45], s[8:9]
	v_mbcnt_lo_u32_b32 v3, vcc_lo, 0
	v_mbcnt_hi_u32_b32 v3, vcc_hi, v3
	v_mbcnt_lo_u32_b32 v3, s44, v3
	s_min_u32 s46, s49, 0x2c0
	v_mbcnt_hi_u32_b32 v3, s45, v3
	s_lshl_b32 s47, s46, 3
	s_sub_i32 s59, 0x2c0, s46
	s_add_i32 s58, s88, s47
	v_cmp_gt_u32_e64 s[46:47], s59, v3
	s_and_b64 s[18:19], s[18:19], s[46:47]
	s_and_saveexec_b64 s[46:47], s[18:19]
	v_lshl_add_u32 v4, v3, 3, s58
	ds_write_b64 v4, v[6:7]
	s_or_b64 exec, exec, s[46:47]
	v_add_u32_e32 v0, v3, v0
	v_cmp_gt_u32_e64 s[46:47], s59, v0
	s_and_b64 s[18:19], s[8:9], s[46:47]
	s_and_saveexec_b64 s[8:9], s[18:19]
	v_lshl_add_u32 v0, v0, 3, s58
	v_add_u32_e32 v4, 0x301, v2
	ds_write_b64 v0, v[4:5]
	s_or_b64 exec, exec, s[8:9]
	s_bcnt1_i32_b64 s8, vcc
	s_bcnt1_i32_b64 s9, s[44:45]
	s_add_i32 s8, s49, s8
	s_add_i32 s49, s8, s9

.LBB0_1167:
	v_and_b32_e32 v7, 0xffff, v54
	v_add_u32_e32 v6, 0x400, v2
	v_lshrrev_b32_e32 v5, 16, v54
	v_cmp_gt_u32_e64 s[44:45], s11, v6
	v_cmp_le_u32_e32 vcc, s93, v7
	v_cmp_le_u32_e64 s[46:47], s93, v5
	s_and_b64 s[18:19], s[44:45], vcc
	v_cndmask_b32_e64 v0, 0, 1, s[18:19]
	s_and_b64 s[8:9], s[44:45], s[46:47]
	s_mov_b64 vcc, s[18:19]
	s_mov_b64 s[44:45], s[8:9]
	v_mbcnt_lo_u32_b32 v3, vcc_lo, 0
	v_mbcnt_hi_u32_b32 v3, vcc_hi, v3
	v_mbcnt_lo_u32_b32 v3, s44, v3
	s_min_u32 s46, s49, 0x2c0
	v_mbcnt_hi_u32_b32 v3, s45, v3
	s_lshl_b32 s47, s46, 3
	s_sub_i32 s59, 0x2c0, s46
	s_add_i32 s58, s88, s47
	v_cmp_gt_u32_e64 s[46:47], s59, v3
	s_and_b64 s[18:19], s[18:19], s[46:47]
	s_and_saveexec_b64 s[46:47], s[18:19]
	v_lshl_add_u32 v4, v3, 3, s58
	ds_write_b64 v4, v[6:7]
	s_or_b64 exec, exec, s[46:47]
	v_add_u32_e32 v0, v3, v0
	v_cmp_gt_u32_e64 s[46:47], s59, v0
	s_and_b64 s[18:19], s[8:9], s[46:47]
	s_and_saveexec_b64 s[8:9], s[18:19]
	v_lshl_add_u32 v0, v0, 3, s58
	v_add_u32_e32 v4, 0x401, v2
	ds_write_b64 v0, v[4:5]
	s_or_b64 exec, exec, s[8:9]
	s_bcnt1_i32_b64 s8, vcc
	s_bcnt1_i32_b64 s9, s[44:45]
	s_add_i32 s8, s49, s8
	s_add_i32 s49, s8, s9

.LBB0_1177:
	v_and_b32_e32 v7, 0xffff, v52
	v_add_u32_e32 v6, 0x500, v2
	v_lshrrev_b32_e32 v5, 16, v52
	v_cmp_gt_u32_e64 s[44:45], s11, v6
	v_cmp_le_u32_e32 vcc, s93, v7
	v_cmp_le_u32_e64 s[46:47], s93, v5
	s_and_b64 s[18:19], s[44:45], vcc
	v_cndmask_b32_e64 v0, 0, 1, s[18:19]
	s_and_b64 s[8:9], s[44:45], s[46:47]
	s_mov_b64 vcc, s[18:19]
	s_mov_b64 s[44:45], s[8:9]
	v_mbcnt_lo_u32_b32 v3, vcc_lo, 0
	v_mbcnt_hi_u32_b32 v3, vcc_hi, v3
	v_mbcnt_lo_u32_b32 v3, s44, v3
	s_min_u32 s46, s49, 0x2c0
	v_mbcnt_hi_u32_b32 v3, s45, v3
	s_lshl_b32 s47, s46, 3
	s_sub_i32 s59, 0x2c0, s46
	s_add_i32 s58, s88, s47
	v_cmp_gt_u32_e64 s[46:47], s59, v3
	s_and_b64 s[18:19], s[18:19], s[46:47]
	s_and_saveexec_b64 s[46:47], s[18:19]
	v_lshl_add_u32 v4, v3, 3, s58
	ds_write_b64 v4, v[6:7]
	s_or_b64 exec, exec, s[46:47]
	v_add_u32_e32 v0, v3, v0
	v_cmp_gt_u32_e64 s[46:47], s59, v0
	s_and_b64 s[18:19], s[8:9], s[46:47]
	s_and_saveexec_b64 s[8:9], s[18:19]
	v_lshl_add_u32 v0, v0, 3, s58
	v_add_u32_e32 v4, 0x501, v2
	ds_write_b64 v0, v[4:5]
	s_or_b64 exec, exec, s[8:9]
	s_bcnt1_i32_b64 s8, vcc
	s_bcnt1_i32_b64 s9, s[44:45]
	s_add_i32 s8, s49, s8
	s_add_i32 s49, s8, s9

.LBB0_1187:
	v_and_b32_e32 v7, 0xffff, v34
	v_add_u32_e32 v6, 0x600, v2
	v_lshrrev_b32_e32 v5, 16, v34
	v_cmp_gt_u32_e64 s[44:45], s11, v6
	v_cmp_le_u32_e32 vcc, s93, v7
	v_cmp_le_u32_e64 s[46:47], s93, v5
	s_and_b64 s[18:19], s[44:45], vcc
	v_cndmask_b32_e64 v0, 0, 1, s[18:19]
	s_and_b64 s[8:9], s[44:45], s[46:47]
	s_mov_b64 vcc, s[18:19]
	s_mov_b64 s[44:45], s[8:9]
	v_mbcnt_lo_u32_b32 v3, vcc_lo, 0
	v_mbcnt_hi_u32_b32 v3, vcc_hi, v3
	v_mbcnt_lo_u32_b32 v3, s44, v3
	s_min_u32 s46, s49, 0x2c0
	v_mbcnt_hi_u32_b32 v3, s45, v3
	s_lshl_b32 s47, s46, 3
	s_sub_i32 s59, 0x2c0, s46
	s_add_i32 s58, s88, s47
	v_cmp_gt_u32_e64 s[46:47], s59, v3
	s_and_b64 s[18:19], s[18:19], s[46:47]
	s_and_saveexec_b64 s[46:47], s[18:19]
	v_lshl_add_u32 v4, v3, 3, s58
	ds_write_b64 v4, v[6:7]
	s_or_b64 exec, exec, s[46:47]
	v_add_u32_e32 v0, v3, v0
	v_cmp_gt_u32_e64 s[46:47], s59, v0
	s_and_b64 s[18:19], s[8:9], s[46:47]
	s_and_saveexec_b64 s[8:9], s[18:19]
	v_lshl_add_u32 v0, v0, 3, s58
	v_add_u32_e32 v4, 0x601, v2
	ds_write_b64 v0, v[4:5]
	s_or_b64 exec, exec, s[8:9]
	s_bcnt1_i32_b64 s8, vcc
	s_bcnt1_i32_b64 s9, s[44:45]
	s_add_i32 s8, s49, s8
	s_add_i32 s49, s8, s9

.LBB0_1197:
	v_and_b32_e32 v7, 0xffff, v32
	v_add_u32_e32 v6, 0x700, v2
	v_lshrrev_b32_e32 v5, 16, v32
	v_cmp_gt_u32_e64 s[44:45], s11, v6
	v_cmp_le_u32_e32 vcc, s93, v7
	v_cmp_le_u32_e64 s[46:47], s93, v5
	s_and_b64 s[18:19], s[44:45], vcc
	v_cndmask_b32_e64 v0, 0, 1, s[18:19]
	s_and_b64 s[8:9], s[44:45], s[46:47]
	s_mov_b64 vcc, s[18:19]
	s_mov_b64 s[44:45], s[8:9]
	v_mbcnt_lo_u32_b32 v3, vcc_lo, 0
	v_mbcnt_hi_u32_b32 v3, vcc_hi, v3
	v_mbcnt_lo_u32_b32 v3, s44, v3
	s_min_u32 s46, s49, 0x2c0
	v_mbcnt_hi_u32_b32 v3, s45, v3
	s_lshl_b32 s47, s46, 3
	s_sub_i32 s59, 0x2c0, s46
	s_add_i32 s58, s88, s47
	v_cmp_gt_u32_e64 s[46:47], s59, v3
	s_and_b64 s[18:19], s[18:19], s[46:47]
	s_and_saveexec_b64 s[46:47], s[18:19]
	v_lshl_add_u32 v4, v3, 3, s58
	ds_write_b64 v4, v[6:7]
	s_or_b64 exec, exec, s[46:47]
	v_add_u32_e32 v0, v3, v0
	v_cmp_gt_u32_e64 s[46:47], s59, v0
	s_and_b64 s[18:19], s[8:9], s[46:47]
	s_and_saveexec_b64 s[8:9], s[18:19]
	v_lshl_add_u32 v0, v0, 3, s58
	v_add_u32_e32 v4, 0x701, v2
	ds_write_b64 v0, v[4:5]
	s_or_b64 exec, exec, s[8:9]
	s_bcnt1_i32_b64 s8, vcc
	s_bcnt1_i32_b64 s9, s[44:45]
	s_add_i32 s8, s49, s8
	s_add_i32 s49, s8, s9

.LBB0_1240:
	v_and_b32_e32 v7, 0xffff, v18
	v_add_u32_e32 v6, 0x100, v2
	v_lshrrev_b32_e32 v5, 16, v18
	v_cmp_gt_u32_e64 s[44:45], s11, v6
	v_cmp_le_u32_e32 vcc, s29, v7
	v_cmp_le_u32_e64 s[46:47], s29, v5
	s_and_b64 s[18:19], s[44:45], vcc
	v_cndmask_b32_e64 v0, 0, 1, s[18:19]
	s_and_b64 s[8:9], s[44:45], s[46:47]
	s_mov_b64 vcc, s[18:19]
	s_mov_b64 s[44:45], s[8:9]
	v_mbcnt_lo_u32_b32 v3, vcc_lo, 0
	v_mbcnt_hi_u32_b32 v3, vcc_hi, v3
	v_mbcnt_lo_u32_b32 v3, s44, v3
	s_min_u32 s26, s28, 0x2c0
	v_mbcnt_hi_u32_b32 v3, s45, v3
	s_sub_i32 s33, 0x2c0, s26
	s_lshl_b32 s27, s26, 3
	v_cmp_gt_u32_e64 s[46:47], s33, v3
	s_add_i32 s31, s88, s27
	s_and_b64 s[18:19], s[18:19], s[46:47]
	s_and_saveexec_b64 s[26:27], s[18:19]
	v_lshl_add_u32 v4, v3, 3, s31
	ds_write_b64 v4, v[6:7]
	s_or_b64 exec, exec, s[26:27]
	v_add_u32_e32 v0, v3, v0
	v_cmp_gt_u32_e64 s[46:47], s33, v0
	s_and_b64 s[18:19], s[8:9], s[46:47]
	s_and_saveexec_b64 s[8:9], s[18:19]
	v_lshl_add_u32 v0, v0, 3, s31
	v_add_u32_e32 v4, 0x101, v2
	ds_write_b64 v0, v[4:5]
	s_or_b64 exec, exec, s[8:9]
	s_bcnt1_i32_b64 s8, vcc
	s_bcnt1_i32_b64 s9, s[44:45]
	s_add_i32 s8, s28, s8
	s_add_i32 s28, s8, s9

.LBB0_1250:
	v_and_b32_e32 v7, 0xffff, v20
	v_add_u32_e32 v6, 0x200, v2
	v_lshrrev_b32_e32 v5, 16, v20
	v_cmp_gt_u32_e64 s[44:45], s11, v6
	v_cmp_le_u32_e32 vcc, s29, v7
	v_cmp_le_u32_e64 s[46:47], s29, v5
	s_and_b64 s[18:19], s[44:45], vcc
	v_cndmask_b32_e64 v0, 0, 1, s[18:19]
	s_and_b64 s[8:9], s[44:45], s[46:47]
	s_mov_b64 vcc, s[18:19]
	s_mov_b64 s[44:45], s[8:9]
	v_mbcnt_lo_u32_b32 v3, vcc_lo, 0
	v_mbcnt_hi_u32_b32 v3, vcc_hi, v3
	v_mbcnt_lo_u32_b32 v3, s44, v3
	s_min_u32 s26, s28, 0x2c0
	v_mbcnt_hi_u32_b32 v3, s45, v3
	s_sub_i32 s33, 0x2c0, s26
	s_lshl_b32 s27, s26, 3
	v_cmp_gt_u32_e64 s[46:47], s33, v3
	s_add_i32 s31, s88, s27
	s_and_b64 s[18:19], s[18:19], s[46:47]
	s_and_saveexec_b64 s[26:27], s[18:19]
	v_lshl_add_u32 v4, v3, 3, s31
	ds_write_b64 v4, v[6:7]
	s_or_b64 exec, exec, s[26:27]
	v_add_u32_e32 v0, v3, v0
	v_cmp_gt_u32_e64 s[46:47], s33, v0
	s_and_b64 s[18:19], s[8:9], s[46:47]
	s_and_saveexec_b64 s[8:9], s[18:19]
	v_lshl_add_u32 v0, v0, 3, s31
	v_add_u32_e32 v4, 0x201, v2
	ds_write_b64 v0, v[4:5]
	s_or_b64 exec, exec, s[8:9]
	s_bcnt1_i32_b64 s8, vcc
	s_bcnt1_i32_b64 s9, s[44:45]
	s_add_i32 s8, s28, s8
	s_add_i32 s28, s8, s9

.LBB0_1260:
	v_and_b32_e32 v7, 0xffff, v22
	v_add_u32_e32 v6, 0x300, v2
	v_lshrrev_b32_e32 v5, 16, v22
	v_cmp_gt_u32_e64 s[44:45], s11, v6
	v_cmp_le_u32_e32 vcc, s29, v7
	v_cmp_le_u32_e64 s[46:47], s29, v5
	s_and_b64 s[18:19], s[44:45], vcc
	v_cndmask_b32_e64 v0, 0, 1, s[18:19]
	s_and_b64 s[8:9], s[44:45], s[46:47]
	s_mov_b64 vcc, s[18:19]
	s_mov_b64 s[44:45], s[8:9]
	v_mbcnt_lo_u32_b32 v3, vcc_lo, 0
	v_mbcnt_hi_u32_b32 v3, vcc_hi, v3
	v_mbcnt_lo_u32_b32 v3, s44, v3
	s_min_u32 s26, s28, 0x2c0
	v_mbcnt_hi_u32_b32 v3, s45, v3
	s_sub_i32 s33, 0x2c0, s26
	s_lshl_b32 s27, s26, 3
	v_cmp_gt_u32_e64 s[46:47], s33, v3
	s_add_i32 s31, s88, s27
	s_and_b64 s[18:19], s[18:19], s[46:47]
	s_and_saveexec_b64 s[26:27], s[18:19]
	v_lshl_add_u32 v4, v3, 3, s31
	ds_write_b64 v4, v[6:7]
	s_or_b64 exec, exec, s[26:27]
	v_add_u32_e32 v0, v3, v0
	v_cmp_gt_u32_e64 s[46:47], s33, v0
	s_and_b64 s[18:19], s[8:9], s[46:47]
	s_and_saveexec_b64 s[8:9], s[18:19]
	v_lshl_add_u32 v0, v0, 3, s31
	v_add_u32_e32 v4, 0x301, v2
	ds_write_b64 v0, v[4:5]
	s_or_b64 exec, exec, s[8:9]
	s_bcnt1_i32_b64 s8, vcc
	s_bcnt1_i32_b64 s9, s[44:45]
	s_add_i32 s8, s28, s8
	s_add_i32 s28, s8, s9

.LBB0_1270:
	v_and_b32_e32 v7, 0xffff, v24
	v_add_u32_e32 v6, 0x400, v2
	v_lshrrev_b32_e32 v5, 16, v24
	v_cmp_gt_u32_e64 s[44:45], s11, v6
	v_cmp_le_u32_e32 vcc, s29, v7
	v_cmp_le_u32_e64 s[46:47], s29, v5
	s_and_b64 s[18:19], s[44:45], vcc
	v_cndmask_b32_e64 v0, 0, 1, s[18:19]
	s_and_b64 s[8:9], s[44:45], s[46:47]
	s_mov_b64 vcc, s[18:19]
	s_mov_b64 s[44:45], s[8:9]
	v_mbcnt_lo_u32_b32 v3, vcc_lo, 0
	v_mbcnt_hi_u32_b32 v3, vcc_hi, v3
	v_mbcnt_lo_u32_b32 v3, s44, v3
	s_min_u32 s26, s28, 0x2c0
	v_mbcnt_hi_u32_b32 v3, s45, v3
	s_sub_i32 s33, 0x2c0, s26
	s_lshl_b32 s27, s26, 3
	v_cmp_gt_u32_e64 s[46:47], s33, v3
	s_add_i32 s31, s88, s27
	s_and_b64 s[18:19], s[18:19], s[46:47]
	s_and_saveexec_b64 s[26:27], s[18:19]
	v_lshl_add_u32 v4, v3, 3, s31
	ds_write_b64 v4, v[6:7]
	s_or_b64 exec, exec, s[26:27]
	v_add_u32_e32 v0, v3, v0
	v_cmp_gt_u32_e64 s[46:47], s33, v0
	s_and_b64 s[18:19], s[8:9], s[46:47]
	s_and_saveexec_b64 s[8:9], s[18:19]
	v_lshl_add_u32 v0, v0, 3, s31
	v_add_u32_e32 v4, 0x401, v2
	ds_write_b64 v0, v[4:5]
	s_or_b64 exec, exec, s[8:9]
	s_bcnt1_i32_b64 s8, vcc
	s_bcnt1_i32_b64 s9, s[44:45]
	s_add_i32 s8, s28, s8
	s_add_i32 s28, s8, s9

.LBB0_1280:
	v_and_b32_e32 v7, 0xffff, v26
	v_add_u32_e32 v6, 0x500, v2
	v_lshrrev_b32_e32 v5, 16, v26
	v_cmp_gt_u32_e64 s[44:45], s11, v6
	v_cmp_le_u32_e32 vcc, s29, v7
	v_cmp_le_u32_e64 s[46:47], s29, v5
	s_and_b64 s[18:19], s[44:45], vcc
	v_cndmask_b32_e64 v0, 0, 1, s[18:19]
	s_and_b64 s[8:9], s[44:45], s[46:47]
	s_mov_b64 vcc, s[18:19]
	s_mov_b64 s[44:45], s[8:9]
	v_mbcnt_lo_u32_b32 v3, vcc_lo, 0
	v_mbcnt_hi_u32_b32 v3, vcc_hi, v3
	v_mbcnt_lo_u32_b32 v3, s44, v3
	s_min_u32 s26, s28, 0x2c0
	v_mbcnt_hi_u32_b32 v3, s45, v3
	s_sub_i32 s33, 0x2c0, s26
	s_lshl_b32 s27, s26, 3
	v_cmp_gt_u32_e64 s[46:47], s33, v3
	s_add_i32 s31, s88, s27
	s_and_b64 s[18:19], s[18:19], s[46:47]
	s_and_saveexec_b64 s[26:27], s[18:19]
	v_lshl_add_u32 v4, v3, 3, s31
	ds_write_b64 v4, v[6:7]
	s_or_b64 exec, exec, s[26:27]
	v_add_u32_e32 v0, v3, v0
	v_cmp_gt_u32_e64 s[46:47], s33, v0
	s_and_b64 s[18:19], s[8:9], s[46:47]
	s_and_saveexec_b64 s[8:9], s[18:19]
	v_lshl_add_u32 v0, v0, 3, s31
	v_add_u32_e32 v4, 0x501, v2
	ds_write_b64 v0, v[4:5]
	s_or_b64 exec, exec, s[8:9]
	s_bcnt1_i32_b64 s8, vcc
	s_bcnt1_i32_b64 s9, s[44:45]
	s_add_i32 s8, s28, s8
	s_add_i32 s28, s8, s9

.LBB0_1290:
	v_and_b32_e32 v7, 0xffff, v28
	v_add_u32_e32 v6, 0x600, v2
	v_lshrrev_b32_e32 v5, 16, v28
	v_cmp_gt_u32_e64 s[44:45], s11, v6
	v_cmp_le_u32_e32 vcc, s29, v7
	v_cmp_le_u32_e64 s[46:47], s29, v5
	s_and_b64 s[18:19], s[44:45], vcc
	v_cndmask_b32_e64 v0, 0, 1, s[18:19]
	s_and_b64 s[8:9], s[44:45], s[46:47]
	s_mov_b64 vcc, s[18:19]
	s_mov_b64 s[44:45], s[8:9]
	v_mbcnt_lo_u32_b32 v3, vcc_lo, 0
	v_mbcnt_hi_u32_b32 v3, vcc_hi, v3
	v_mbcnt_lo_u32_b32 v3, s44, v3
	s_min_u32 s26, s28, 0x2c0
	v_mbcnt_hi_u32_b32 v3, s45, v3
	s_sub_i32 s33, 0x2c0, s26
	s_lshl_b32 s27, s26, 3
	v_cmp_gt_u32_e64 s[46:47], s33, v3
	s_add_i32 s31, s88, s27
	s_and_b64 s[18:19], s[18:19], s[46:47]
	s_and_saveexec_b64 s[26:27], s[18:19]
	v_lshl_add_u32 v4, v3, 3, s31
	ds_write_b64 v4, v[6:7]
	s_or_b64 exec, exec, s[26:27]
	v_add_u32_e32 v0, v3, v0
	v_cmp_gt_u32_e64 s[46:47], s33, v0
	s_and_b64 s[18:19], s[8:9], s[46:47]
	s_and_saveexec_b64 s[8:9], s[18:19]
	v_lshl_add_u32 v0, v0, 3, s31
	v_add_u32_e32 v4, 0x601, v2
	ds_write_b64 v0, v[4:5]
	s_or_b64 exec, exec, s[8:9]
	s_bcnt1_i32_b64 s8, vcc
	s_bcnt1_i32_b64 s9, s[44:45]
	s_add_i32 s8, s28, s8
	s_add_i32 s28, s8, s9

.LBB0_1300:
	v_and_b32_e32 v7, 0xffff, v30
	v_add_u32_e32 v6, 0x700, v2
	v_lshrrev_b32_e32 v5, 16, v30
	v_cmp_gt_u32_e64 s[44:45], s11, v6
	v_cmp_le_u32_e32 vcc, s29, v7
	v_cmp_le_u32_e64 s[46:47], s29, v5
	s_and_b64 s[18:19], s[44:45], vcc
	v_cndmask_b32_e64 v0, 0, 1, s[18:19]
	s_and_b64 s[8:9], s[44:45], s[46:47]
	s_mov_b64 vcc, s[18:19]
	s_mov_b64 s[44:45], s[8:9]
	v_mbcnt_lo_u32_b32 v3, vcc_lo, 0
	v_mbcnt_hi_u32_b32 v3, vcc_hi, v3
	v_mbcnt_lo_u32_b32 v3, s44, v3
	s_min_u32 s26, s28, 0x2c0
	v_mbcnt_hi_u32_b32 v3, s45, v3
	s_sub_i32 s33, 0x2c0, s26
	s_lshl_b32 s27, s26, 3
	v_cmp_gt_u32_e64 s[46:47], s33, v3
	s_add_i32 s31, s88, s27
	s_and_b64 s[18:19], s[18:19], s[46:47]
	s_and_saveexec_b64 s[26:27], s[18:19]
	v_lshl_add_u32 v4, v3, 3, s31
	ds_write_b64 v4, v[6:7]
	s_or_b64 exec, exec, s[26:27]
	v_add_u32_e32 v0, v3, v0
	v_cmp_gt_u32_e64 s[46:47], s33, v0
	s_and_b64 s[18:19], s[8:9], s[46:47]
	s_and_saveexec_b64 s[8:9], s[18:19]
	v_lshl_add_u32 v0, v0, 3, s31
	v_add_u32_e32 v4, 0x701, v2
	ds_write_b64 v0, v[4:5]
	s_or_b64 exec, exec, s[8:9]
	s_bcnt1_i32_b64 s8, vcc
	s_bcnt1_i32_b64 s9, s[44:45]
	s_add_i32 s8, s28, s8
	s_add_i32 s28, s8, s9
